# hand-written loop heads for the two full-tile attention loops (fewer SALU, rare cases out of line, no m0 save/restore)
# speedup vs baseline: 1.0139x; 1.0048x over previous
.LBB0_696:
	s_mul_i32 s26, s60, 0x5400
	s_add_i32 s27, s26, s36
	s_add_i32 s28, s26, s59
	s_and_b64 s[10:11], s[12:13], exec
	s_cselect_b32 s10, s28, s37
	s_add_i32 s11, s26, s58
	s_mov_b32 m0, s27
	s_nop 0
	global_load_lds_dwordx4 v200, s[16:17]
	s_mov_b32 m0, s10
	s_or_b64 exec, s[12:13], 1
	global_load_lds_dwordx4 v201, s[16:17]
	s_mov_b64 exec, -1
	s_mov_b32 m0, s11
	s_nop 0
	global_load_lds_dwordx4 v198, s[18:19]
	s_andn2_b64 vcc, exec, s[20:21]
	s_cbranch_vccnz .LBB0_706
	s_add_i32 s57, s57, -1
	s_cmp_lg_u32 s57, 0
	s_cbranch_scc0 .Lmla_f_adv
	s_add_u32 s16, s16, 0x21000
	s_addc_u32 s17, s17, 0
	s_add_u32 s18, s18, 0x21000
	s_addc_u32 s19, s19, 0
	s_add_i32 s10, s68, s73
	s_and_b32 s10, s10, 7
	s_cmp_lg_u32 s10, 0
	s_cbranch_scc0 .LBB0_706
	s_mov_b64 s[10:11], -1
	s_branch .LBB0_719
.Lmla_f_adv:
	s_add_i32 s26, s54, 1
	s_bitcmp0_b32 s54, 0
	v_readlane_b32 s11, v252, 25
	s_mul_i32 s10, s26, s78
	s_cselect_b32 s20, s11, s82
	s_add_i32 s20, s20, s10
	s_cmpk_lt_i32 s20, 0x800
	s_cselect_b64 s[10:11], -1, 0
	s_cmpk_gt_i32 s20, 0x7ff
	s_cbranch_scc1 .LBB0_702
	s_lshl_b32 s1, s20, 5
	s_and_b32 s1, s1, 0xf00
	s_bfe_u32 s0, s20, 0x40007
	s_sub_i32 s1, 0x1000, s1
	s_ashr_i32 s55, s1, 6
	s_mul_i32 s0, s0, 0x840000
	s_add_u32 s0, s62, s0
	s_addc_u32 s1, s63, 0
	s_lshl_b32 s14, s20, 8
	s_and_b32 s56, s14, 0x700
	s_add_u32 s14, s0, s56
	s_addc_u32 s15, s1, 0
	s_add_u32 s14, s14, 0x80
	s_addc_u32 s15, s15, 0

.LBB0_840:
	s_mul_i32 s2, s91, 0x4400
	s_add_i32 s3, s2, s81
	s_add_i32 s4, s2, s33
	s_and_b64 s[0:1], s[96:97], exec
	s_cselect_b32 s0, s4, s71
	s_add_i32 s1, s2, s70
	s_mov_b32 m0, s3
	s_nop 0
	global_load_lds_dwordx4 v1, s[92:93]
	s_mov_b32 m0, s0
	s_or_b64 exec, s[96:97], 1
	global_load_lds_dwordx4 v198, s[92:93]
	s_mov_b64 exec, -1
	s_mov_b32 m0, s1
	s_nop 0
	global_load_lds_dwordx4 v199, s[76:77]
	s_mov_b64 s[0:1], 0
	s_andn2_b64 vcc, exec, s[72:73]
	s_cbranch_vccnz .LBB0_851
	s_add_i32 s69, s69, -1
	s_cmp_lg_u32 s69, 0
	s_cbranch_scc0 .Ldiff_f_adv
	s_add_u32 s92, s92, 0x40000
	s_addc_u32 s93, s93, 0
	s_add_u32 s76, s76, 0x40000
	s_addc_u32 s77, s77, 0
	s_branch .LBB0_851
.Ldiff_f_adv:
	v_readlane_b32 s2, v255, 15
	s_add_i32 s4, s90, 1
	v_readlane_b32 s3, v255, 16
	s_bitcmp0_b32 s90, 0
	v_readlane_b32 s3, v252, 25
	s_mul_i32 s2, s4, s2
	s_cselect_b32 s5, s3, s82
	s_add_i32 s5, s5, s2
	s_cmpk_lt_i32 s5, 0x800
	s_cselect_b64 s[2:3], -1, 0
	s_cmpk_gt_i32 s5, 0x7ff
	s_cbranch_scc1 .LBB0_846
	s_lshl_b32 s6, s5, 5
	s_and_b32 s6, s6, 0xf00
	s_sub_i32 s6, 0x1000, s6
	s_ashr_i32 s16, s6, 6
	s_lshl_b32 s6, s5, 17
	s_and_b32 s6, s6, 0xf000000
	v_readlane_b32 s12, v255, 31
	v_readlane_b32 s13, v255, 32
	s_add_u32 s6, s12, s6
	s_addc_u32 s7, s13, 0
	s_lshl_b32 s5, s5, 7
	s_and_b32 s5, s5, 0x380
	s_add_u32 s5, s6, s5
	s_addc_u32 s6, s7, 0
	s_add_u32 s12, s5, 0x400
	s_addc_u32 s13, s6, 0
	v_writelane_b32 v255, s12, 33
	s_add_u32 s78, s5, 0x800
	s_addc_u32 s79, s6, 0
	v_writelane_b32 v255, s13, 34
.LBB0_846:
	s_andn2_b64 vcc, exec, s[2:3]
	s_cbranch_vccnz .LBB0_850
	v_readlane_b32 s92, v255, 33
	s_mov_b32 s90, s4
	v_readlane_b32 s93, v255, 34
	s_mov_b64 s[76:77], s[78:79]
	s_mov_b32 s69, s16
	s_branch .LBB0_851
.LBB0_850:
	s_mov_b64 s[72:73], 0
	s_mov_b32 s69, 0
